# P1 PEER-table side job: 2-stage software pipeline (next row's 16 loads issued before processing current row)
# baseline (speedup 1.0000x reference)
; __device__ __forceinline__ void pt_load(const float* tu, const float* tv, f32x4* v, int r, int lane) {
;     const f32x4* sp = (const f32x4*)(((r >> 14) ? tv : tu) + (size_t)(r & 16383) * D) + lane;
; #pragma unroll
;     for (int j = 0; j < 16; ++j) v[j] = sp[64 * j];
; }
.LBB0_202:
	s_and_b32 s10, s25, 0x3fff000
	s_add_i32 s30, s66, s23
	s_lshl_b32 s36, s10, 2
	s_cmpk_lt_u32 s30, 0x4000
	s_cselect_b64 s[10:11], -1, 0
	s_and_b64 s[34:35], s[10:11], exec
	s_cselect_b32 s34, s12, s14
	s_cselect_b32 s35, s13, s15
	s_cselect_b32 s31, 0, 0x4000000
	s_add_u32 s34, s34, s36
	s_addc_u32 s35, s35, 0
	v_lshlrev_b32_e32 v204, 4, v194
	s_movk_i32 s36, 0x2000
	v_lshl_add_u64 v[2:3], s[34:35], 0, v[204:205]
	v_add_co_u32_e32 v4, vcc, s36, v2
	global_load_dwordx4 v[68:71], v204, s[34:35]
	global_load_dwordx4 v[72:75], v204, s[34:35] offset:1024
	global_load_dwordx4 v[54:57], v204, s[34:35] offset:2048
	global_load_dwordx4 v[50:53], v204, s[34:35] offset:3072
	v_addc_co_u32_e32 v5, vcc, 0, v3, vcc
	global_load_dwordx4 v[46:49], v[4:5], off offset:-4096
	s_movk_i32 s37, 0x1000
	v_add_co_u32_e32 v6, vcc, s37, v2
	s_movk_i32 s34, 0x3000
	s_nop 0
	v_addc_co_u32_e32 v7, vcc, 0, v3, vcc
	global_load_dwordx4 v[42:45], v[6:7], off offset:1024
	global_load_dwordx4 v[38:41], v[6:7], off offset:2048
	global_load_dwordx4 v[34:37], v[6:7], off offset:3072
	global_load_dwordx4 v[30:33], v[4:5], off
	global_load_dwordx4 v[26:29], v[4:5], off offset:1024
	global_load_dwordx4 v[22:25], v[4:5], off offset:2048
	v_add_co_u32_e32 v2, vcc, s34, v2
	v_lshlrev_b32_e32 v204, 2, v194
	s_nop 0
	v_addc_co_u32_e32 v3, vcc, 0, v3, vcc
	global_load_dwordx4 v[18:21], v[4:5], off offset:3072
	global_load_dwordx4 v[14:17], v[2:3], off
	global_load_dwordx4 v[10:13], v[2:3], off offset:1024
	global_load_dwordx4 v[6:9], v[2:3], off offset:2048
	s_nop 0
	global_load_dwordx4 v[2:5], v[2:3], off offset:3072
	global_load_dword v247, v204, s[12:13]
	global_load_dword v247, v204, s[12:13]
	global_load_dword v247, v204, s[12:13]
	global_load_dword v247, v204, s[12:13]
	global_load_dword v247, v204, s[12:13]
	global_load_dword v247, v204, s[12:13]
	global_load_dword v247, v204, s[12:13]
	global_load_dword v247, v204, s[12:13]
	global_load_dword v247, v204, s[12:13]
	global_load_dword v247, v204, s[12:13]
	global_load_dword v247, v204, s[12:13]
	global_load_dword v247, v204, s[12:13]
	global_load_dword v247, v204, s[12:13]
	global_load_dword v247, v204, s[12:13]
	global_load_dword v247, v204, s[12:13]
	global_load_dword v247, v204, s[12:13]
	global_load_dword v247, v204, s[12:13]
.Lside_loop:
	s_add_i32 s23, s23, 8
	s_add_i32 s25, s25, 0x8000
	s_and_b32 s38, s25, 0x3fff000
	s_add_i32 s40, s66, s23
	s_lshl_b32 s36, s38, 2
	s_cmpk_lt_u32 s40, 0x4000
	s_cselect_b64 s[38:39], -1, 0
	s_and_b64 s[34:35], s[38:39], exec
	s_cselect_b32 s34, s12, s14
	s_cselect_b32 s35, s13, s15
	s_cselect_b32 s41, 0, 0x4000000
	s_add_u32 s34, s34, s36
	s_addc_u32 s35, s35, 0
	v_lshlrev_b32_e32 v204, 4, v194
	s_movk_i32 s36, 0x2000
	v_lshl_add_u64 v[136:137], s[34:35], 0, v[204:205]
	v_add_co_u32_e32 v138, vcc, s36, v136
	global_load_dwordx4 v[216:219], v204, s[34:35]
	global_load_dwordx4 v[220:223], v204, s[34:35] offset:1024
	global_load_dwordx4 v[188:191], v204, s[34:35] offset:2048
	global_load_dwordx4 v[184:187], v204, s[34:35] offset:3072
	v_addc_co_u32_e32 v139, vcc, 0, v137, vcc
	global_load_dwordx4 v[180:183], v[138:139], off offset:-4096
	s_movk_i32 s37, 0x1000
	v_add_co_u32_e32 v140, vcc, s37, v136
	s_movk_i32 s34, 0x3000
	s_nop 0
	v_addc_co_u32_e32 v141, vcc, 0, v137, vcc
	global_load_dwordx4 v[176:179], v[140:141], off offset:1024
	global_load_dwordx4 v[172:175], v[140:141], off offset:2048
	global_load_dwordx4 v[168:171], v[140:141], off offset:3072
	global_load_dwordx4 v[164:167], v[138:139], off
	global_load_dwordx4 v[160:163], v[138:139], off offset:1024
	global_load_dwordx4 v[156:159], v[138:139], off offset:2048
	v_add_co_u32_e32 v136, vcc, s34, v136
	v_lshlrev_b32_e32 v204, 2, v194
	s_nop 0
	v_addc_co_u32_e32 v137, vcc, 0, v137, vcc
	global_load_dwordx4 v[152:155], v[138:139], off offset:3072
	global_load_dwordx4 v[148:151], v[136:137], off
	global_load_dwordx4 v[144:147], v[136:137], off offset:1024
	global_load_dwordx4 v[140:143], v[136:137], off offset:2048
	s_nop 0
	global_load_dwordx4 v[136:139], v[136:137], off offset:3072
	s_waitcnt vmcnt(48)
	v_max_f32_e64 v58, |v69|, |v69|
	v_max_f32_e64 v59, |v68|, |v68|
	v_max_f32_e64 v66, |v71|, |v71|
	v_max_f32_e64 v67, |v70|, |v70|
	s_waitcnt vmcnt(47)
	v_max_f32_e64 v76, |v73|, |v73|
	v_max_f32_e64 v77, |v72|, |v72|
	v_max_f32_e64 v78, |v75|, |v75|
	v_max_f32_e64 v79, |v74|, |v74|
	v_max_f32_e32 v58, v59, v58
	v_max_f32_e32 v59, v67, v66
	s_waitcnt vmcnt(46)
	v_max_f32_e64 v80, |v55|, |v55|
	v_max_f32_e64 v81, |v54|, |v54|
	v_max_f32_e64 v82, |v57|, |v57|
	v_max_f32_e64 v83, |v56|, |v56|
	v_max_f32_e32 v66, v77, v76
	v_max_f32_e32 v67, v79, v78
	v_max3_f32 v58, v58, 0, v59
	s_waitcnt vmcnt(45)
	v_max_f32_e64 v84, |v51|, |v51|
	v_max_f32_e64 v85, |v50|, |v50|
	v_max_f32_e64 v86, |v53|, |v53|
	v_max_f32_e64 v87, |v52|, |v52|
	v_max_f32_e32 v76, v81, v80
	v_max_f32_e32 v77, v83, v82
	v_max3_f32 v58, v58, v66, v67
	v_max_f32_e32 v78, v85, v84
	v_max_f32_e32 v79, v87, v86
	s_waitcnt vmcnt(44)
	v_max_f32_e64 v59, |v47|, |v47|
	v_max_f32_e64 v80, |v46|, |v46|
	v_max_f32_e64 v81, |v49|, |v49|
	v_max_f32_e64 v82, |v48|, |v48|
	v_max3_f32 v58, v58, v76, v77
	s_waitcnt vmcnt(43)
	v_max_f32_e64 v83, |v43|, |v43|
	v_max_f32_e64 v84, |v42|, |v42|
	v_max_f32_e64 v85, |v45|, |v45|
	v_max_f32_e64 v86, |v44|, |v44|
	v_max_f32_e32 v59, v80, v59
	v_max_f32_e32 v66, v82, v81
	v_max3_f32 v58, v58, v78, v79
	s_waitcnt vmcnt(42)
	v_max_f32_e64 v87, |v39|, |v39|
	v_max_f32_e64 v88, |v38|, |v38|
	v_max_f32_e64 v89, |v41|, |v41|
	v_max_f32_e64 v90, |v40|, |v40|
	v_max_f32_e32 v67, v84, v83
	v_max_f32_e32 v80, v86, v85
	v_max3_f32 v58, v58, v59, v66
	s_waitcnt vmcnt(41)
; __device__ __forceinline__ float wave_max(float v) {
; #pragma unroll
;     for (int o = 1; o < 64; o <<= 1) v = fmaxf(v, __shfl_xor(v, o));
;     return v;
; __device__ __forceinline__ void pt_proc(unsigned char* PT, const f32x4* v, int r, int lane) {
;     const int tb = r >> 14, e = r & 16383; unsigned char* tab = PT + (tb ? PT_V8 : 0); float amax = 0.f;
; #pragma unroll
;     for (int j = 0; j < 16; ++j) amax = fmaxf(fmaxf(amax, fmaxf(fabsf(v[j].x), fabsf(v[j].y))), fmaxf(fabsf(v[j].z), fabsf(v[j].w)));
;     amax = wave_max(amax); const float scale = amax > 0.f ? 127.f / amax : 0.f;
; #pragma unroll
;     for (int j = 0; j < 16; ++j) ((unsigned*)(tab + (size_t)j * PT_SLICE + (size_t)e * 256))[lane] = pack_i8x4(v[j].x * scale, v[j].y * scale, v[j].z * scale, v[j].w * scale);
	v_max_f32_e64 v91, |v35|, |v35|
	v_max_f32_e64 v92, |v34|, |v34|
	v_max_f32_e64 v93, |v37|, |v37|
	v_max_f32_e64 v94, |v36|, |v36|
	v_max_f32_e32 v81, v88, v87
	v_max_f32_e32 v82, v90, v89
	v_max3_f32 v58, v58, v67, v80
	s_waitcnt vmcnt(40)
	v_max_f32_e64 v95, |v31|, |v31|
	v_max_f32_e32 v83, v92, v91
	v_max_f32_e32 v84, v94, v93
	v_max3_f32 v58, v58, v81, v82
	v_max_f32_e64 v59, |v30|, |v30|
	v_max_f32_e64 v66, |v33|, |v33|
	v_max_f32_e64 v67, |v32|, |v32|
	v_max3_f32 v58, v58, v83, v84
	v_max_f32_e32 v59, v59, v95
	v_max_f32_e32 v66, v67, v66
	v_max3_f32 v58, v58, v59, v66
	s_waitcnt vmcnt(39)
	v_max_f32_e64 v59, |v27|, |v27|
	v_max_f32_e64 v66, |v26|, |v26|
	v_max_f32_e32 v59, v66, v59
	v_max_f32_e64 v66, |v29|, |v29|
	v_max_f32_e64 v67, |v28|, |v28|
	v_max_f32_e32 v66, v67, v66
	v_max3_f32 v58, v58, v59, v66
	s_waitcnt vmcnt(38)
	v_max_f32_e64 v59, |v23|, |v23|
	v_max_f32_e64 v66, |v22|, |v22|
	v_max_f32_e32 v59, v66, v59
	v_max_f32_e64 v66, |v25|, |v25|
	v_max_f32_e64 v67, |v24|, |v24|
	v_max_f32_e32 v66, v67, v66
	v_max3_f32 v58, v58, v59, v66
	s_waitcnt vmcnt(37)
	v_max_f32_e64 v59, |v19|, |v19|
	v_max_f32_e64 v66, |v18|, |v18|
	v_max_f32_e32 v59, v66, v59
	v_max_f32_e64 v66, |v21|, |v21|
	v_max_f32_e64 v67, |v20|, |v20|
	v_max_f32_e32 v66, v67, v66
	v_max3_f32 v58, v58, v59, v66
	s_waitcnt vmcnt(36)
	v_max_f32_e64 v59, |v15|, |v15|
	v_max_f32_e64 v66, |v14|, |v14|
	v_max_f32_e32 v59, v66, v59
	v_max_f32_e64 v66, |v17|, |v17|
	v_max_f32_e64 v67, |v16|, |v16|
	v_max_f32_e32 v66, v67, v66
	v_max3_f32 v58, v58, v59, v66
	s_waitcnt vmcnt(35)
	v_max_f32_e64 v59, |v11|, |v11|
	v_max_f32_e64 v66, |v10|, |v10|
	v_max_f32_e32 v59, v66, v59
	v_max_f32_e64 v66, |v13|, |v13|
	v_max_f32_e64 v67, |v12|, |v12|
	v_max_f32_e32 v66, v67, v66
	v_max3_f32 v58, v58, v59, v66
	s_waitcnt vmcnt(34)
	v_max_f32_e64 v59, |v7|, |v7|
	v_max_f32_e64 v66, |v6|, |v6|
	v_max_f32_e32 v59, v66, v59
	v_max_f32_e64 v66, |v9|, |v9|
	v_max_f32_e64 v67, |v8|, |v8|
	v_max_f32_e32 v66, v67, v66
	v_max3_f32 v58, v58, v59, v66
	s_waitcnt vmcnt(33)
	v_max_f32_e64 v59, |v3|, |v3|
	v_max_f32_e64 v66, |v2|, |v2|
	v_max_f32_e32 v59, v66, v59
	v_max_f32_e64 v66, |v5|, |v5|
	v_max_f32_e64 v67, |v4|, |v4|
	v_max_f32_e32 v66, v67, v66
	v_max3_f32 v58, v58, v59, v66
	ds_bpermute_b32 v59, v60, v58
	s_waitcnt lgkmcnt(0)
	v_max_f32_e32 v59, v59, v59
	v_max_f32_e32 v58, v58, v59
	ds_bpermute_b32 v59, v61, v58
	s_waitcnt lgkmcnt(0)
	v_max_f32_e32 v59, v59, v59
	v_max_f32_e32 v58, v58, v59
	ds_bpermute_b32 v59, v62, v58
	s_waitcnt lgkmcnt(0)
	v_max_f32_e32 v59, v59, v59
	v_max_f32_e32 v58, v58, v59
	ds_bpermute_b32 v59, v63, v58
	s_waitcnt lgkmcnt(0)
	v_max_f32_e32 v59, v59, v59
	v_max_f32_e32 v58, v58, v59
	ds_bpermute_b32 v59, v64, v58
	s_waitcnt lgkmcnt(0)
	v_max_f32_e32 v59, v59, v59
	v_max_f32_e32 v58, v58, v59
	ds_bpermute_b32 v59, v65, v58
	s_waitcnt lgkmcnt(0)
	v_max_f32_e32 v59, v59, v59
	v_max_f32_e32 v66, v58, v59
	v_div_scale_f32 v58, s[34:35], v66, v66, s69
	v_rcp_f32_e32 v59, v58
	s_and_b32 s34, s30, 0x3fff
	s_add_u32 s30, s33, s31
	s_addc_u32 s31, s46, 0
	v_fma_f32 v67, -v58, v59, 1.0
	v_fmac_f32_e32 v59, v67, v59
	v_div_scale_f32 v67, vcc, s69, v66, s69
	v_mul_f32_e32 v76, v67, v59
	v_fma_f32 v77, -v58, v76, v67
	v_fmac_f32_e32 v76, v77, v59
	v_fma_f32 v58, -v58, v76, v67
	v_div_fmas_f32 v58, v58, v59, v76
	v_div_fixup_f32 v58, v58, v66, s69
	v_cmp_lt_f32_e32 vcc, 0, v66
	s_lshl_b32 s35, s34, 8
	s_add_u32 s30, s30, s35
	v_cndmask_b32_e32 v67, 0, v58, vcc
	v_mul_f32_e32 v69, v69, v67
	v_mul_f32_e32 v68, v68, v67
	v_mul_f32_e32 v70, v70, v67
	v_mul_f32_e32 v71, v71, v67
	v_rndne_f32_e32 v69, v69
	v_rndne_f32_e32 v68, v68
	v_cvt_i32_f32_e32 v69, v69
	v_rndne_f32_e32 v70, v70
	v_rndne_f32_e32 v71, v71
	v_cvt_i32_f32_e32 v68, v68
	v_cvt_i32_f32_sdwa v70, v70 dst_sel:WORD_1 dst_unused:UNUSED_PAD src0_sel:DWORD
	v_cvt_i32_f32_e32 v71, v71
	v_lshlrev_b32_e32 v69, 8, v69
	v_and_b32_e32 v69, 0xff00, v69
	v_and_b32_e32 v70, 0xff0000, v70
	v_perm_b32 v68, v71, v68, s70
	s_addc_u32 s31, s31, 0
	v_or3_b32 v68, v68, v69, v70
	v_mul_f32_e32 v69, v73, v67
	global_store_dword v204, v68, s[30:31]
	v_mul_f32_e32 v68, v72, v67
	v_mul_f32_e32 v70, v74, v67
	v_mul_f32_e32 v71, v75, v67
	v_rndne_f32_e32 v69, v69
	v_rndne_f32_e32 v68, v68
	v_cvt_i32_f32_e32 v69, v69
	v_rndne_f32_e32 v70, v70
	v_rndne_f32_e32 v71, v71
	v_mul_f32_e32 v55, v55, v67
	v_cvt_i32_f32_e32 v68, v68
	v_cvt_i32_f32_sdwa v70, v70 dst_sel:WORD_1 dst_unused:UNUSED_PAD src0_sel:DWORD
	v_cvt_i32_f32_e32 v71, v71
	v_mul_f32_e32 v54, v54, v67
	v_mul_f32_e32 v56, v56, v67
	v_mul_f32_e32 v57, v57, v67
	v_rndne_f32_e32 v55, v55
	v_rndne_f32_e32 v54, v54
	v_cvt_i32_f32_e32 v55, v55
	v_rndne_f32_e32 v56, v56
	v_rndne_f32_e32 v57, v57
	v_mul_f32_e32 v51, v51, v67
	v_cvt_i32_f32_e32 v54, v54
	v_cvt_i32_f32_sdwa v56, v56 dst_sel:WORD_1 dst_unused:UNUSED_PAD src0_sel:DWORD
	v_cvt_i32_f32_e32 v57, v57
	v_mul_f32_e32 v50, v50, v67
	v_mul_f32_e32 v52, v52, v67
	v_mul_f32_e32 v53, v53, v67
	v_rndne_f32_e32 v51, v51
	v_lshlrev_b32_e32 v69, 8, v69
	v_rndne_f32_e32 v50, v50
	v_cvt_i32_f32_e32 v51, v51
	v_rndne_f32_e32 v52, v52
	v_rndne_f32_e32 v53, v53
	v_mul_f32_e32 v47, v47, v67
	v_lshl_add_u64 v[58:59], s[30:31], 0, v[204:205]
	v_and_b32_e32 v69, 0xff00, v69
	v_and_b32_e32 v70, 0xff0000, v70
	v_perm_b32 v68, v71, v68, s70
	s_mov_b32 s30, 0x400000
	v_cvt_i32_f32_e32 v50, v50
	v_cvt_i32_f32_sdwa v52, v52 dst_sel:WORD_1 dst_unused:UNUSED_PAD src0_sel:DWORD
	v_cvt_i32_f32_e32 v53, v53
	v_mul_f32_e32 v46, v46, v67
	v_mul_f32_e32 v48, v48, v67
	v_mul_f32_e32 v49, v49, v67
	v_rndne_f32_e32 v47, v47
	v_or3_b32 v70, v68, v69, v70
	v_add_co_u32_e32 v68, vcc, s30, v58
; __device__ __forceinline__ unsigned pack_i8x4(float a, float b, float c, float d) {
;     const int ia = (int)__builtin_rintf(a), ib = (int)__builtin_rintf(b), ic = (int)__builtin_rintf(c), id = (int)__builtin_rintf(d);
;     return ((unsigned)ia & 255u) | (((unsigned)ib & 255u) << 8) | (((unsigned)ic & 255u) << 16) | ((unsigned)id << 24);
; }
; __device__ __forceinline__ void pt_proc(unsigned char* PT, const f32x4* v, int r, int lane) {
;     ...
; #pragma unroll
;     for (int j = 0; j < 16; ++j) ((unsigned*)(tab + (size_t)j * PT_SLICE + (size_t)e * 256))[lane] = pack_i8x4(v[j].x * scale, v[j].y * scale, v[j].z * scale, v[j].w * scale);
	v_lshlrev_b32_e32 v55, 8, v55
	v_rndne_f32_e32 v46, v46
	v_cvt_i32_f32_e32 v47, v47
	v_rndne_f32_e32 v48, v48
	v_rndne_f32_e32 v49, v49
	v_mul_f32_e32 v43, v43, v67
	v_addc_co_u32_e32 v69, vcc, 0, v59, vcc
	v_and_b32_e32 v55, 0xff00, v55
	v_and_b32_e32 v56, 0xff0000, v56
	v_perm_b32 v54, v57, v54, s70
	s_mov_b32 s30, 0x800000
	v_cvt_i32_f32_e32 v46, v46
	v_cvt_i32_f32_sdwa v48, v48 dst_sel:WORD_1 dst_unused:UNUSED_PAD src0_sel:DWORD
	v_cvt_i32_f32_e32 v49, v49
	v_mul_f32_e32 v42, v42, v67
	v_mul_f32_e32 v44, v44, v67
	v_mul_f32_e32 v45, v45, v67
	v_rndne_f32_e32 v43, v43
	v_or3_b32 v56, v54, v55, v56
	v_add_co_u32_e32 v54, vcc, s30, v58
	v_lshlrev_b32_e32 v51, 8, v51
	v_rndne_f32_e32 v42, v42
	v_cvt_i32_f32_e32 v43, v43
	v_rndne_f32_e32 v44, v44
	v_rndne_f32_e32 v45, v45
	v_mul_f32_e32 v39, v39, v67
	v_addc_co_u32_e32 v55, vcc, 0, v59, vcc
	v_and_b32_e32 v51, 0xff00, v51
	v_and_b32_e32 v52, 0xff0000, v52
	v_perm_b32 v50, v53, v50, s70
	s_mov_b32 s30, 0xc00000
	v_cvt_i32_f32_e32 v42, v42
	v_cvt_i32_f32_sdwa v44, v44 dst_sel:WORD_1 dst_unused:UNUSED_PAD src0_sel:DWORD
	v_cvt_i32_f32_e32 v45, v45
	v_mul_f32_e32 v38, v38, v67
	v_mul_f32_e32 v40, v40, v67
	v_mul_f32_e32 v41, v41, v67
	v_rndne_f32_e32 v39, v39
	v_or3_b32 v52, v50, v51, v52
	v_add_co_u32_e32 v50, vcc, s30, v58
	v_lshlrev_b32_e32 v47, 8, v47
	v_rndne_f32_e32 v38, v38
	v_cvt_i32_f32_e32 v39, v39
	v_rndne_f32_e32 v40, v40
	v_rndne_f32_e32 v41, v41
	v_mul_f32_e32 v35, v35, v67
	v_addc_co_u32_e32 v51, vcc, 0, v59, vcc
	v_and_b32_e32 v47, 0xff00, v47
	v_and_b32_e32 v48, 0xff0000, v48
	v_perm_b32 v46, v49, v46, s70
	s_mov_b32 s30, 0x1000000
	v_cvt_i32_f32_e32 v38, v38
	v_cvt_i32_f32_sdwa v40, v40 dst_sel:WORD_1 dst_unused:UNUSED_PAD src0_sel:DWORD
	v_cvt_i32_f32_e32 v41, v41
	v_mul_f32_e32 v34, v34, v67
	v_mul_f32_e32 v36, v36, v67
	v_mul_f32_e32 v37, v37, v67
	v_rndne_f32_e32 v35, v35
	v_or3_b32 v48, v46, v47, v48
	v_add_co_u32_e32 v46, vcc, s30, v58
	v_lshlrev_b32_e32 v43, 8, v43
	v_rndne_f32_e32 v34, v34
	v_cvt_i32_f32_e32 v35, v35
	v_rndne_f32_e32 v36, v36
	v_rndne_f32_e32 v37, v37
	v_mul_f32_e32 v31, v31, v67
	v_addc_co_u32_e32 v47, vcc, 0, v59, vcc
	v_and_b32_e32 v43, 0xff00, v43
	v_and_b32_e32 v44, 0xff0000, v44
	v_perm_b32 v42, v45, v42, s70
	s_mov_b32 s30, 0x1400000
	v_cvt_i32_f32_e32 v34, v34
	v_cvt_i32_f32_sdwa v36, v36 dst_sel:WORD_1 dst_unused:UNUSED_PAD src0_sel:DWORD
	v_cvt_i32_f32_e32 v37, v37
	v_mul_f32_e32 v30, v30, v67
	v_mul_f32_e32 v32, v32, v67
	v_mul_f32_e32 v33, v33, v67
	v_rndne_f32_e32 v31, v31
	v_or3_b32 v44, v42, v43, v44
	v_add_co_u32_e32 v42, vcc, s30, v58
	v_lshlrev_b32_e32 v39, 8, v39
	v_rndne_f32_e32 v30, v30
	v_cvt_i32_f32_e32 v31, v31
	v_rndne_f32_e32 v32, v32
	v_rndne_f32_e32 v33, v33
	v_mul_f32_e32 v27, v27, v67
	v_addc_co_u32_e32 v43, vcc, 0, v59, vcc
	v_and_b32_e32 v39, 0xff00, v39
	v_and_b32_e32 v40, 0xff0000, v40
	v_perm_b32 v38, v41, v38, s70
	s_mov_b32 s30, 0x1800000
	v_cvt_i32_f32_e32 v30, v30
	v_cvt_i32_f32_sdwa v32, v32 dst_sel:WORD_1 dst_unused:UNUSED_PAD src0_sel:DWORD
	v_cvt_i32_f32_e32 v33, v33
	v_mul_f32_e32 v26, v26, v67
	v_mul_f32_e32 v28, v28, v67
	v_mul_f32_e32 v29, v29, v67
	v_rndne_f32_e32 v27, v27
	v_or3_b32 v40, v38, v39, v40
	v_add_co_u32_e32 v38, vcc, s30, v58
	v_lshlrev_b32_e32 v35, 8, v35
	v_rndne_f32_e32 v26, v26
	v_cvt_i32_f32_e32 v27, v27
	v_rndne_f32_e32 v28, v28
	v_rndne_f32_e32 v29, v29
	v_mul_f32_e32 v23, v23, v67
	v_addc_co_u32_e32 v39, vcc, 0, v59, vcc
	v_and_b32_e32 v35, 0xff00, v35
	v_and_b32_e32 v36, 0xff0000, v36
	v_perm_b32 v34, v37, v34, s70
	s_mov_b32 s30, 0x1c00000
	v_cvt_i32_f32_e32 v26, v26
	v_cvt_i32_f32_sdwa v28, v28 dst_sel:WORD_1 dst_unused:UNUSED_PAD src0_sel:DWORD
	v_cvt_i32_f32_e32 v29, v29
	v_mul_f32_e32 v22, v22, v67
	v_mul_f32_e32 v24, v24, v67
	v_mul_f32_e32 v25, v25, v67
	v_rndne_f32_e32 v23, v23
	v_or3_b32 v36, v34, v35, v36
	v_add_co_u32_e32 v34, vcc, s30, v58
	v_lshlrev_b32_e32 v31, 8, v31
	v_rndne_f32_e32 v22, v22
	v_cvt_i32_f32_e32 v23, v23
	v_rndne_f32_e32 v24, v24
	v_rndne_f32_e32 v25, v25
	v_mul_f32_e32 v19, v19, v67
	v_addc_co_u32_e32 v35, vcc, 0, v59, vcc
	v_and_b32_e32 v31, 0xff00, v31
	v_and_b32_e32 v32, 0xff0000, v32
	v_perm_b32 v30, v33, v30, s70
	s_brev_b32 s30, 64
	v_cvt_i32_f32_e32 v22, v22
	v_cvt_i32_f32_sdwa v24, v24 dst_sel:WORD_1 dst_unused:UNUSED_PAD src0_sel:DWORD
	v_cvt_i32_f32_e32 v25, v25
	v_mul_f32_e32 v18, v18, v67
	v_mul_f32_e32 v20, v20, v67
	v_mul_f32_e32 v21, v21, v67
	v_rndne_f32_e32 v19, v19
	v_or3_b32 v32, v30, v31, v32
	v_add_co_u32_e32 v30, vcc, s30, v58
	v_lshlrev_b32_e32 v27, 8, v27
	v_rndne_f32_e32 v18, v18
	v_cvt_i32_f32_e32 v19, v19
	v_rndne_f32_e32 v20, v20
	v_rndne_f32_e32 v21, v21
	v_mul_f32_e32 v15, v15, v67
	v_addc_co_u32_e32 v31, vcc, 0, v59, vcc
	v_and_b32_e32 v27, 0xff00, v27
	v_and_b32_e32 v28, 0xff0000, v28
	v_perm_b32 v26, v29, v26, s70
	s_mov_b32 s30, 0x2400000
	v_cvt_i32_f32_e32 v18, v18
	v_cvt_i32_f32_sdwa v20, v20 dst_sel:WORD_1 dst_unused:UNUSED_PAD src0_sel:DWORD
	v_cvt_i32_f32_e32 v21, v21
	v_mul_f32_e32 v14, v14, v67
	v_mul_f32_e32 v16, v16, v67
	v_mul_f32_e32 v17, v17, v67
	v_rndne_f32_e32 v15, v15
	v_or3_b32 v28, v26, v27, v28
	v_add_co_u32_e32 v26, vcc, s30, v58
	v_lshlrev_b32_e32 v23, 8, v23
	v_rndne_f32_e32 v14, v14
	v_cvt_i32_f32_e32 v15, v15
	v_rndne_f32_e32 v16, v16
	v_rndne_f32_e32 v17, v17
	v_mul_f32_e32 v11, v11, v67
	v_addc_co_u32_e32 v27, vcc, 0, v59, vcc
	v_and_b32_e32 v23, 0xff00, v23
	v_and_b32_e32 v24, 0xff0000, v24
	v_perm_b32 v22, v25, v22, s70
	s_mov_b32 s30, 0x2800000
	v_cvt_i32_f32_e32 v14, v14
	v_cvt_i32_f32_sdwa v16, v16 dst_sel:WORD_1 dst_unused:UNUSED_PAD src0_sel:DWORD
	v_cvt_i32_f32_e32 v17, v17
; __device__ __forceinline__ void pt_proc(unsigned char* PT, const f32x4* v, int r, int lane) {
;     ...
; #pragma unroll
;     for (int j = 0; j < 16; ++j) ((unsigned*)(tab + (size_t)j * PT_SLICE + (size_t)e * 256))[lane] = pack_i8x4(v[j].x * scale, v[j].y * scale, v[j].z * scale, v[j].w * scale);
;     if (lane == 0) ((float*)(PT + (tb ? PT_VS : PT_US)))[e] = amax * (1.f / 127.f);
	v_mul_f32_e32 v10, v10, v67
	v_mul_f32_e32 v12, v12, v67
	v_mul_f32_e32 v13, v13, v67
	v_rndne_f32_e32 v11, v11
	v_or3_b32 v24, v22, v23, v24
	v_add_co_u32_e32 v22, vcc, s30, v58
	v_lshlrev_b32_e32 v19, 8, v19
	v_rndne_f32_e32 v10, v10
	v_cvt_i32_f32_e32 v11, v11
	v_rndne_f32_e32 v12, v12
	v_rndne_f32_e32 v13, v13
	v_mul_f32_e32 v7, v7, v67
	v_addc_co_u32_e32 v23, vcc, 0, v59, vcc
	v_and_b32_e32 v19, 0xff00, v19
	v_and_b32_e32 v20, 0xff0000, v20
	v_perm_b32 v18, v21, v18, s70
	v_cvt_i32_f32_e32 v10, v10
	v_cvt_i32_f32_sdwa v12, v12 dst_sel:WORD_1 dst_unused:UNUSED_PAD src0_sel:DWORD
	v_cvt_i32_f32_e32 v13, v13
	v_mul_f32_e32 v6, v6, v67
	v_mul_f32_e32 v8, v8, v67
	v_mul_f32_e32 v9, v9, v67
	v_rndne_f32_e32 v7, v7
	v_or3_b32 v20, v18, v19, v20
	v_add_co_u32_e32 v18, vcc, s71, v58
	v_lshlrev_b32_e32 v15, 8, v15
	v_rndne_f32_e32 v6, v6
	v_cvt_i32_f32_e32 v7, v7
	v_rndne_f32_e32 v8, v8
	v_rndne_f32_e32 v9, v9
	v_mul_f32_e32 v3, v3, v67
	v_addc_co_u32_e32 v19, vcc, 0, v59, vcc
	v_and_b32_e32 v15, 0xff00, v15
	v_and_b32_e32 v16, 0xff0000, v16
	v_perm_b32 v14, v17, v14, s70
	v_cvt_i32_f32_e32 v6, v6
	v_cvt_i32_f32_sdwa v8, v8 dst_sel:WORD_1 dst_unused:UNUSED_PAD src0_sel:DWORD
	v_cvt_i32_f32_e32 v9, v9
	v_mul_f32_e32 v2, v2, v67
	v_mul_f32_e32 v4, v4, v67
	v_mul_f32_e32 v5, v5, v67
	v_rndne_f32_e32 v3, v3
	v_or3_b32 v16, v14, v15, v16
	v_add_co_u32_e32 v14, vcc, s72, v58
	v_lshlrev_b32_e32 v11, 8, v11
	v_rndne_f32_e32 v2, v2
	v_cvt_i32_f32_e32 v3, v3
	v_rndne_f32_e32 v4, v4
	v_rndne_f32_e32 v5, v5
	v_addc_co_u32_e32 v15, vcc, 0, v59, vcc
	v_and_b32_e32 v11, 0xff00, v11
	v_and_b32_e32 v12, 0xff0000, v12
	v_perm_b32 v10, v13, v10, s70
	v_cvt_i32_f32_e32 v2, v2
	v_cvt_i32_f32_sdwa v4, v4 dst_sel:WORD_1 dst_unused:UNUSED_PAD src0_sel:DWORD
	v_cvt_i32_f32_e32 v5, v5
	v_or3_b32 v12, v10, v11, v12
	v_add_co_u32_e32 v10, vcc, s73, v58
	v_lshlrev_b32_e32 v7, 8, v7
	s_nop 0
	v_addc_co_u32_e32 v11, vcc, 0, v59, vcc
	v_and_b32_e32 v7, 0xff00, v7
	v_and_b32_e32 v8, 0xff0000, v8
	v_perm_b32 v6, v9, v6, s70
	v_or3_b32 v8, v6, v7, v8
	v_add_co_u32_e32 v6, vcc, s74, v58
	v_lshlrev_b32_e32 v3, 8, v3
	s_nop 0
	v_addc_co_u32_e32 v7, vcc, 0, v59, vcc
	v_and_b32_e32 v3, 0xff00, v3
	v_and_b32_e32 v4, 0xff0000, v4
	v_perm_b32 v2, v5, v2, s70
	v_or3_b32 v4, v2, v3, v4
	v_add_co_u32_e32 v2, vcc, 0x3c00000, v58
	global_store_dword v[68:69], v70, off
	s_nop 0
	v_addc_co_u32_e32 v3, vcc, 0, v59, vcc
	global_store_dword v[54:55], v56, off
	global_store_dword v[50:51], v52, off
	global_store_dword v[46:47], v48, off
	global_store_dword v[42:43], v44, off
	global_store_dword v[38:39], v40, off
	global_store_dword v[34:35], v36, off
	global_store_dword v[30:31], v32, off
	global_store_dword v[26:27], v28, off
	global_store_dword v[22:23], v24, off
	global_store_dword v[18:19], v20, off
	global_store_dword v[14:15], v16, off
	global_store_dword v[10:11], v12, off
	global_store_dword v[6:7], v8, off
	global_store_dword v[2:3], v4, off
	s_and_saveexec_b64 s[30:31], s[6:7]
	s_cbranch_execz .Lside_jA
	s_and_b64 s[10:11], s[10:11], exec
	s_cselect_b32 s10, s75, 0x8010000
	s_add_u32 s10, s33, s10
	s_addc_u32 s11, s46, 0
	s_lshl_b32 s34, s34, 2
	v_mul_f32_e32 v2, 0x3c010204, v66
	v_mov_b32_e32 v3, s34
	global_store_dword v3, v2, s[10:11]
	s_branch .Lside_jA
.Lside_jA:
	s_or_b64 exec, exec, s[30:31]
	s_add_i32 s23, s23, 8
	s_add_i32 s25, s25, 0x8000
	s_cmp_eq_u32 s23, 64
	s_cbranch_scc1 .Lside_last
	s_and_b32 s10, s25, 0x3fff000
	s_add_i32 s30, s66, s23
	s_lshl_b32 s36, s10, 2
	s_cmpk_lt_u32 s30, 0x4000
	s_cselect_b64 s[10:11], -1, 0
	s_and_b64 s[34:35], s[10:11], exec
	s_cselect_b32 s34, s12, s14
	s_cselect_b32 s35, s13, s15
	s_cselect_b32 s31, 0, 0x4000000
	s_add_u32 s34, s34, s36
	s_addc_u32 s35, s35, 0
	v_lshlrev_b32_e32 v204, 4, v194
	s_movk_i32 s36, 0x2000
	v_lshl_add_u64 v[2:3], s[34:35], 0, v[204:205]
	v_add_co_u32_e32 v4, vcc, s36, v2
	global_load_dwordx4 v[68:71], v204, s[34:35]
	global_load_dwordx4 v[72:75], v204, s[34:35] offset:1024
	global_load_dwordx4 v[54:57], v204, s[34:35] offset:2048
	global_load_dwordx4 v[50:53], v204, s[34:35] offset:3072
	v_addc_co_u32_e32 v5, vcc, 0, v3, vcc
	global_load_dwordx4 v[46:49], v[4:5], off offset:-4096
	s_movk_i32 s37, 0x1000
	v_add_co_u32_e32 v6, vcc, s37, v2
	s_movk_i32 s34, 0x3000
	s_nop 0
	v_addc_co_u32_e32 v7, vcc, 0, v3, vcc
	global_load_dwordx4 v[42:45], v[6:7], off offset:1024
	global_load_dwordx4 v[38:41], v[6:7], off offset:2048
	global_load_dwordx4 v[34:37], v[6:7], off offset:3072
	global_load_dwordx4 v[30:33], v[4:5], off
	global_load_dwordx4 v[26:29], v[4:5], off offset:1024
	global_load_dwordx4 v[22:25], v[4:5], off offset:2048
	v_add_co_u32_e32 v2, vcc, s34, v2
	v_lshlrev_b32_e32 v204, 2, v194
	s_nop 0
	v_addc_co_u32_e32 v3, vcc, 0, v3, vcc
	global_load_dwordx4 v[18:21], v[4:5], off offset:3072
	global_load_dwordx4 v[14:17], v[2:3], off
	global_load_dwordx4 v[10:13], v[2:3], off offset:1024
	global_load_dwordx4 v[6:9], v[2:3], off offset:2048
	s_nop 0
	global_load_dwordx4 v[2:5], v[2:3], off offset:3072
	s_branch .Lside_pB
.Lside_last:
	global_load_dword v247, v204, s[12:13]
	global_load_dword v247, v204, s[12:13]
	global_load_dword v247, v204, s[12:13]
	global_load_dword v247, v204, s[12:13]
	global_load_dword v247, v204, s[12:13]
	global_load_dword v247, v204, s[12:13]
	global_load_dword v247, v204, s[12:13]
	global_load_dword v247, v204, s[12:13]
	global_load_dword v247, v204, s[12:13]
	global_load_dword v247, v204, s[12:13]
	global_load_dword v247, v204, s[12:13]
	global_load_dword v247, v204, s[12:13]
	global_load_dword v247, v204, s[12:13]
	global_load_dword v247, v204, s[12:13]
	global_load_dword v247, v204, s[12:13]
	global_load_dword v247, v204, s[12:13]
; __device__ __forceinline__ void pt_proc(unsigned char* PT, const f32x4* v, int r, int lane) {
;     const int tb = r >> 14, e = r & 16383; unsigned char* tab = PT + (tb ? PT_V8 : 0); float amax = 0.f;
; #pragma unroll
;     for (int j = 0; j < 16; ++j) amax = fmaxf(fmaxf(amax, fmaxf(fabsf(v[j].x), fabsf(v[j].y))), fmaxf(fabsf(v[j].z), fabsf(v[j].w)));
;     amax = wave_max(amax); const float scale = amax > 0.f ? 127.f / amax : 0.f;
.Lside_pB:
	s_waitcnt vmcnt(48)
	v_max_f32_e64 v58, |v217|, |v217|
	v_max_f32_e64 v59, |v216|, |v216|
	v_max_f32_e64 v66, |v219|, |v219|
	v_max_f32_e64 v67, |v218|, |v218|
	s_waitcnt vmcnt(47)
	v_max_f32_e64 v76, |v221|, |v221|
	v_max_f32_e64 v77, |v220|, |v220|
	v_max_f32_e64 v78, |v223|, |v223|
	v_max_f32_e64 v79, |v222|, |v222|
	v_max_f32_e32 v58, v59, v58
	v_max_f32_e32 v59, v67, v66
	s_waitcnt vmcnt(46)
	v_max_f32_e64 v80, |v189|, |v189|
	v_max_f32_e64 v81, |v188|, |v188|
	v_max_f32_e64 v82, |v191|, |v191|
	v_max_f32_e64 v83, |v190|, |v190|
	v_max_f32_e32 v66, v77, v76
	v_max_f32_e32 v67, v79, v78
	v_max3_f32 v58, v58, 0, v59
	s_waitcnt vmcnt(45)
	v_max_f32_e64 v84, |v185|, |v185|
	v_max_f32_e64 v85, |v184|, |v184|
	v_max_f32_e64 v86, |v187|, |v187|
	v_max_f32_e64 v87, |v186|, |v186|
	v_max_f32_e32 v76, v81, v80
	v_max_f32_e32 v77, v83, v82
	v_max3_f32 v58, v58, v66, v67
	v_max_f32_e32 v78, v85, v84
	v_max_f32_e32 v79, v87, v86
	s_waitcnt vmcnt(44)
	v_max_f32_e64 v59, |v181|, |v181|
	v_max_f32_e64 v80, |v180|, |v180|
	v_max_f32_e64 v81, |v183|, |v183|
	v_max_f32_e64 v82, |v182|, |v182|
	v_max3_f32 v58, v58, v76, v77
	s_waitcnt vmcnt(43)
	v_max_f32_e64 v83, |v177|, |v177|
	v_max_f32_e64 v84, |v176|, |v176|
	v_max_f32_e64 v85, |v179|, |v179|
	v_max_f32_e64 v86, |v178|, |v178|
	v_max_f32_e32 v59, v80, v59
	v_max_f32_e32 v66, v82, v81
	v_max3_f32 v58, v58, v78, v79
	s_waitcnt vmcnt(42)
	v_max_f32_e64 v87, |v173|, |v173|
	v_max_f32_e64 v88, |v172|, |v172|
	v_max_f32_e64 v89, |v175|, |v175|
	v_max_f32_e64 v90, |v174|, |v174|
	v_max_f32_e32 v67, v84, v83
	v_max_f32_e32 v80, v86, v85
	v_max3_f32 v58, v58, v59, v66
	s_waitcnt vmcnt(41)
	v_max_f32_e64 v91, |v169|, |v169|
	v_max_f32_e64 v92, |v168|, |v168|
	v_max_f32_e64 v93, |v171|, |v171|
	v_max_f32_e64 v94, |v170|, |v170|
	v_max_f32_e32 v81, v88, v87
	v_max_f32_e32 v82, v90, v89
	v_max3_f32 v58, v58, v67, v80
	s_waitcnt vmcnt(40)
	v_max_f32_e64 v95, |v165|, |v165|
	v_max_f32_e32 v83, v92, v91
	v_max_f32_e32 v84, v94, v93
	v_max3_f32 v58, v58, v81, v82
	v_max_f32_e64 v59, |v164|, |v164|
	v_max_f32_e64 v66, |v167|, |v167|
	v_max_f32_e64 v67, |v166|, |v166|
	v_max3_f32 v58, v58, v83, v84
	v_max_f32_e32 v59, v59, v95
	v_max_f32_e32 v66, v67, v66
	v_max3_f32 v58, v58, v59, v66
	s_waitcnt vmcnt(39)
	v_max_f32_e64 v59, |v161|, |v161|
	v_max_f32_e64 v66, |v160|, |v160|
	v_max_f32_e32 v59, v66, v59
	v_max_f32_e64 v66, |v163|, |v163|
	v_max_f32_e64 v67, |v162|, |v162|
	v_max_f32_e32 v66, v67, v66
	v_max3_f32 v58, v58, v59, v66
	s_waitcnt vmcnt(38)
	v_max_f32_e64 v59, |v157|, |v157|
	v_max_f32_e64 v66, |v156|, |v156|
	v_max_f32_e32 v59, v66, v59
	v_max_f32_e64 v66, |v159|, |v159|
	v_max_f32_e64 v67, |v158|, |v158|
	v_max_f32_e32 v66, v67, v66
	v_max3_f32 v58, v58, v59, v66
	s_waitcnt vmcnt(37)
	v_max_f32_e64 v59, |v153|, |v153|
	v_max_f32_e64 v66, |v152|, |v152|
	v_max_f32_e32 v59, v66, v59
	v_max_f32_e64 v66, |v155|, |v155|
	v_max_f32_e64 v67, |v154|, |v154|
	v_max_f32_e32 v66, v67, v66
	v_max3_f32 v58, v58, v59, v66
	s_waitcnt vmcnt(36)
	v_max_f32_e64 v59, |v149|, |v149|
	v_max_f32_e64 v66, |v148|, |v148|
	v_max_f32_e32 v59, v66, v59
	v_max_f32_e64 v66, |v151|, |v151|
	v_max_f32_e64 v67, |v150|, |v150|
	v_max_f32_e32 v66, v67, v66
	v_max3_f32 v58, v58, v59, v66
	s_waitcnt vmcnt(35)
	v_max_f32_e64 v59, |v145|, |v145|
	v_max_f32_e64 v66, |v144|, |v144|
	v_max_f32_e32 v59, v66, v59
	v_max_f32_e64 v66, |v147|, |v147|
	v_max_f32_e64 v67, |v146|, |v146|
	v_max_f32_e32 v66, v67, v66
	v_max3_f32 v58, v58, v59, v66
	s_waitcnt vmcnt(34)
	v_max_f32_e64 v59, |v141|, |v141|
	v_max_f32_e64 v66, |v140|, |v140|
	v_max_f32_e32 v59, v66, v59
	v_max_f32_e64 v66, |v143|, |v143|
	v_max_f32_e64 v67, |v142|, |v142|
	v_max_f32_e32 v66, v67, v66
	v_max3_f32 v58, v58, v59, v66
	s_waitcnt vmcnt(33)
	v_max_f32_e64 v59, |v137|, |v137|
	v_max_f32_e64 v66, |v136|, |v136|
	v_max_f32_e32 v59, v66, v59
	v_max_f32_e64 v66, |v139|, |v139|
	v_max_f32_e64 v67, |v138|, |v138|
	v_max_f32_e32 v66, v67, v66
	v_max3_f32 v58, v58, v59, v66
	ds_bpermute_b32 v59, v60, v58
	s_waitcnt lgkmcnt(0)
	v_max_f32_e32 v59, v59, v59
	v_max_f32_e32 v58, v58, v59
	ds_bpermute_b32 v59, v61, v58
	s_waitcnt lgkmcnt(0)
	v_max_f32_e32 v59, v59, v59
	v_max_f32_e32 v58, v58, v59
	ds_bpermute_b32 v59, v62, v58
	s_waitcnt lgkmcnt(0)
	v_max_f32_e32 v59, v59, v59
	v_max_f32_e32 v58, v58, v59
	ds_bpermute_b32 v59, v63, v58
	s_waitcnt lgkmcnt(0)
	v_max_f32_e32 v59, v59, v59
	v_max_f32_e32 v58, v58, v59
	ds_bpermute_b32 v59, v64, v58
	s_waitcnt lgkmcnt(0)
	v_max_f32_e32 v59, v59, v59
	v_max_f32_e32 v58, v58, v59
	ds_bpermute_b32 v59, v65, v58
	s_waitcnt lgkmcnt(0)
; __device__ __forceinline__ void pt_proc(unsigned char* PT, const f32x4* v, int r, int lane) {
;     ...
;     amax = wave_max(amax); const float scale = amax > 0.f ? 127.f / amax : 0.f;
; #pragma unroll
;     for (int j = 0; j < 16; ++j) ((unsigned*)(tab + (size_t)j * PT_SLICE + (size_t)e * 256))[lane] = pack_i8x4(v[j].x * scale, v[j].y * scale, v[j].z * scale, v[j].w * scale);
	v_max_f32_e32 v59, v59, v59
	v_max_f32_e32 v66, v58, v59
	v_div_scale_f32 v58, s[34:35], v66, v66, s69
	v_rcp_f32_e32 v59, v58
	s_and_b32 s34, s40, 0x3fff
	s_add_u32 s40, s33, s41
	s_addc_u32 s41, s46, 0
	v_fma_f32 v67, -v58, v59, 1.0
	v_fmac_f32_e32 v59, v67, v59
	v_div_scale_f32 v67, vcc, s69, v66, s69
	v_mul_f32_e32 v76, v67, v59
	v_fma_f32 v77, -v58, v76, v67
	v_fmac_f32_e32 v76, v77, v59
	v_fma_f32 v58, -v58, v76, v67
	v_div_fmas_f32 v58, v58, v59, v76
	v_div_fixup_f32 v58, v58, v66, s69
	v_cmp_lt_f32_e32 vcc, 0, v66
	s_lshl_b32 s35, s34, 8
	s_add_u32 s40, s40, s35
	v_cndmask_b32_e32 v67, 0, v58, vcc
	v_mul_f32_e32 v217, v217, v67
	v_mul_f32_e32 v216, v216, v67
	v_mul_f32_e32 v218, v218, v67
	v_mul_f32_e32 v219, v219, v67
	v_rndne_f32_e32 v217, v217
	v_rndne_f32_e32 v216, v216
	v_cvt_i32_f32_e32 v217, v217
	v_rndne_f32_e32 v218, v218
	v_rndne_f32_e32 v219, v219
	v_cvt_i32_f32_e32 v216, v216
	v_cvt_i32_f32_sdwa v218, v218 dst_sel:WORD_1 dst_unused:UNUSED_PAD src0_sel:DWORD
	v_cvt_i32_f32_e32 v219, v219
	v_lshlrev_b32_e32 v217, 8, v217
	v_and_b32_e32 v217, 0xff00, v217
	v_and_b32_e32 v218, 0xff0000, v218
	v_perm_b32 v216, v219, v216, s70
	s_addc_u32 s41, s41, 0
	v_or3_b32 v216, v216, v217, v218
	v_mul_f32_e32 v217, v221, v67
	global_store_dword v204, v216, s[40:41]
	v_mul_f32_e32 v216, v220, v67
	v_mul_f32_e32 v218, v222, v67
	v_mul_f32_e32 v219, v223, v67
	v_rndne_f32_e32 v217, v217
	v_rndne_f32_e32 v216, v216
	v_cvt_i32_f32_e32 v217, v217
	v_rndne_f32_e32 v218, v218
	v_rndne_f32_e32 v219, v219
	v_mul_f32_e32 v189, v189, v67
	v_cvt_i32_f32_e32 v216, v216
	v_cvt_i32_f32_sdwa v218, v218 dst_sel:WORD_1 dst_unused:UNUSED_PAD src0_sel:DWORD
	v_cvt_i32_f32_e32 v219, v219
	v_mul_f32_e32 v188, v188, v67
	v_mul_f32_e32 v190, v190, v67
	v_mul_f32_e32 v191, v191, v67
	v_rndne_f32_e32 v189, v189
	v_rndne_f32_e32 v188, v188
	v_cvt_i32_f32_e32 v189, v189
	v_rndne_f32_e32 v190, v190
	v_rndne_f32_e32 v191, v191
	v_mul_f32_e32 v185, v185, v67
	v_cvt_i32_f32_e32 v188, v188
	v_cvt_i32_f32_sdwa v190, v190 dst_sel:WORD_1 dst_unused:UNUSED_PAD src0_sel:DWORD
	v_cvt_i32_f32_e32 v191, v191
	v_mul_f32_e32 v184, v184, v67
	v_mul_f32_e32 v186, v186, v67
	v_mul_f32_e32 v187, v187, v67
	v_rndne_f32_e32 v185, v185
	v_lshlrev_b32_e32 v217, 8, v217
	v_rndne_f32_e32 v184, v184
	v_cvt_i32_f32_e32 v185, v185
	v_rndne_f32_e32 v186, v186
	v_rndne_f32_e32 v187, v187
	v_mul_f32_e32 v181, v181, v67
	v_lshl_add_u64 v[58:59], s[40:41], 0, v[204:205]
	v_and_b32_e32 v217, 0xff00, v217
	v_and_b32_e32 v218, 0xff0000, v218
	v_perm_b32 v216, v219, v216, s70
	s_mov_b32 s40, 0x400000
	v_cvt_i32_f32_e32 v184, v184
	v_cvt_i32_f32_sdwa v186, v186 dst_sel:WORD_1 dst_unused:UNUSED_PAD src0_sel:DWORD
	v_cvt_i32_f32_e32 v187, v187
	v_mul_f32_e32 v180, v180, v67
	v_mul_f32_e32 v182, v182, v67
	v_mul_f32_e32 v183, v183, v67
	v_rndne_f32_e32 v181, v181
	v_or3_b32 v218, v216, v217, v218
	v_add_co_u32_e32 v216, vcc, s40, v58
	v_lshlrev_b32_e32 v189, 8, v189
	v_rndne_f32_e32 v180, v180
	v_cvt_i32_f32_e32 v181, v181
	v_rndne_f32_e32 v182, v182
	v_rndne_f32_e32 v183, v183
	v_mul_f32_e32 v177, v177, v67
	v_addc_co_u32_e32 v217, vcc, 0, v59, vcc
	v_and_b32_e32 v189, 0xff00, v189
	v_and_b32_e32 v190, 0xff0000, v190
	v_perm_b32 v188, v191, v188, s70
	s_mov_b32 s40, 0x800000
	v_cvt_i32_f32_e32 v180, v180
	v_cvt_i32_f32_sdwa v182, v182 dst_sel:WORD_1 dst_unused:UNUSED_PAD src0_sel:DWORD
	v_cvt_i32_f32_e32 v183, v183
	v_mul_f32_e32 v176, v176, v67
	v_mul_f32_e32 v178, v178, v67
	v_mul_f32_e32 v179, v179, v67
	v_rndne_f32_e32 v177, v177
	v_or3_b32 v190, v188, v189, v190
	v_add_co_u32_e32 v188, vcc, s40, v58
	v_lshlrev_b32_e32 v185, 8, v185
	v_rndne_f32_e32 v176, v176
	v_cvt_i32_f32_e32 v177, v177
	v_rndne_f32_e32 v178, v178
	v_rndne_f32_e32 v179, v179
	v_mul_f32_e32 v173, v173, v67
	v_addc_co_u32_e32 v189, vcc, 0, v59, vcc
	v_and_b32_e32 v185, 0xff00, v185
	v_and_b32_e32 v186, 0xff0000, v186
	v_perm_b32 v184, v187, v184, s70
	s_mov_b32 s40, 0xc00000
	v_cvt_i32_f32_e32 v176, v176
	v_cvt_i32_f32_sdwa v178, v178 dst_sel:WORD_1 dst_unused:UNUSED_PAD src0_sel:DWORD
	v_cvt_i32_f32_e32 v179, v179
	v_mul_f32_e32 v172, v172, v67
	v_mul_f32_e32 v174, v174, v67
	v_mul_f32_e32 v175, v175, v67
	v_rndne_f32_e32 v173, v173
	v_or3_b32 v186, v184, v185, v186
	v_add_co_u32_e32 v184, vcc, s40, v58
	v_lshlrev_b32_e32 v181, 8, v181
	v_rndne_f32_e32 v172, v172
	v_cvt_i32_f32_e32 v173, v173
	v_rndne_f32_e32 v174, v174
	v_rndne_f32_e32 v175, v175
	v_mul_f32_e32 v169, v169, v67
	v_addc_co_u32_e32 v185, vcc, 0, v59, vcc
	v_and_b32_e32 v181, 0xff00, v181
	v_and_b32_e32 v182, 0xff0000, v182
	v_perm_b32 v180, v183, v180, s70
	s_mov_b32 s40, 0x1000000
	v_cvt_i32_f32_e32 v172, v172
	v_cvt_i32_f32_sdwa v174, v174 dst_sel:WORD_1 dst_unused:UNUSED_PAD src0_sel:DWORD
	v_cvt_i32_f32_e32 v175, v175
	v_mul_f32_e32 v168, v168, v67
	v_mul_f32_e32 v170, v170, v67
	v_mul_f32_e32 v171, v171, v67
	v_rndne_f32_e32 v169, v169
	v_or3_b32 v182, v180, v181, v182
	v_add_co_u32_e32 v180, vcc, s40, v58
	v_lshlrev_b32_e32 v177, 8, v177
	v_rndne_f32_e32 v168, v168
	v_cvt_i32_f32_e32 v169, v169
	v_rndne_f32_e32 v170, v170
	v_rndne_f32_e32 v171, v171
	v_mul_f32_e32 v165, v165, v67
	v_addc_co_u32_e32 v181, vcc, 0, v59, vcc
	v_and_b32_e32 v177, 0xff00, v177
	v_and_b32_e32 v178, 0xff0000, v178
	v_perm_b32 v176, v179, v176, s70
	s_mov_b32 s40, 0x1400000
	v_cvt_i32_f32_e32 v168, v168
	v_cvt_i32_f32_sdwa v170, v170 dst_sel:WORD_1 dst_unused:UNUSED_PAD src0_sel:DWORD
	v_cvt_i32_f32_e32 v171, v171
	v_mul_f32_e32 v164, v164, v67
	v_mul_f32_e32 v166, v166, v67
	v_mul_f32_e32 v167, v167, v67
	v_rndne_f32_e32 v165, v165
	v_or3_b32 v178, v176, v177, v178
; __device__ __forceinline__ void pt_proc(unsigned char* PT, const f32x4* v, int r, int lane) {
;     ...
; #pragma unroll
;     for (int j = 0; j < 16; ++j) ((unsigned*)(tab + (size_t)j * PT_SLICE + (size_t)e * 256))[lane] = pack_i8x4(v[j].x * scale, v[j].y * scale, v[j].z * scale, v[j].w * scale);
;     if (lane == 0) ((float*)(PT + (tb ? PT_VS : PT_US)))[e] = amax * (1.f / 127.f);
	v_add_co_u32_e32 v176, vcc, s40, v58
	v_lshlrev_b32_e32 v173, 8, v173
	v_rndne_f32_e32 v164, v164
	v_cvt_i32_f32_e32 v165, v165
	v_rndne_f32_e32 v166, v166
	v_rndne_f32_e32 v167, v167
	v_mul_f32_e32 v161, v161, v67
	v_addc_co_u32_e32 v177, vcc, 0, v59, vcc
	v_and_b32_e32 v173, 0xff00, v173
	v_and_b32_e32 v174, 0xff0000, v174
	v_perm_b32 v172, v175, v172, s70
	s_mov_b32 s40, 0x1800000
	v_cvt_i32_f32_e32 v164, v164
	v_cvt_i32_f32_sdwa v166, v166 dst_sel:WORD_1 dst_unused:UNUSED_PAD src0_sel:DWORD
	v_cvt_i32_f32_e32 v167, v167
	v_mul_f32_e32 v160, v160, v67
	v_mul_f32_e32 v162, v162, v67
	v_mul_f32_e32 v163, v163, v67
	v_rndne_f32_e32 v161, v161
	v_or3_b32 v174, v172, v173, v174
	v_add_co_u32_e32 v172, vcc, s40, v58
	v_lshlrev_b32_e32 v169, 8, v169
	v_rndne_f32_e32 v160, v160
	v_cvt_i32_f32_e32 v161, v161
	v_rndne_f32_e32 v162, v162
	v_rndne_f32_e32 v163, v163
	v_mul_f32_e32 v157, v157, v67
	v_addc_co_u32_e32 v173, vcc, 0, v59, vcc
	v_and_b32_e32 v169, 0xff00, v169
	v_and_b32_e32 v170, 0xff0000, v170
	v_perm_b32 v168, v171, v168, s70
	s_mov_b32 s40, 0x1c00000
	v_cvt_i32_f32_e32 v160, v160
	v_cvt_i32_f32_sdwa v162, v162 dst_sel:WORD_1 dst_unused:UNUSED_PAD src0_sel:DWORD
	v_cvt_i32_f32_e32 v163, v163
	v_mul_f32_e32 v156, v156, v67
	v_mul_f32_e32 v158, v158, v67
	v_mul_f32_e32 v159, v159, v67
	v_rndne_f32_e32 v157, v157
	v_or3_b32 v170, v168, v169, v170
	v_add_co_u32_e32 v168, vcc, s40, v58
	v_lshlrev_b32_e32 v165, 8, v165
	v_rndne_f32_e32 v156, v156
	v_cvt_i32_f32_e32 v157, v157
	v_rndne_f32_e32 v158, v158
	v_rndne_f32_e32 v159, v159
	v_mul_f32_e32 v153, v153, v67
	v_addc_co_u32_e32 v169, vcc, 0, v59, vcc
	v_and_b32_e32 v165, 0xff00, v165
	v_and_b32_e32 v166, 0xff0000, v166
	v_perm_b32 v164, v167, v164, s70
	s_brev_b32 s40, 64
	v_cvt_i32_f32_e32 v156, v156
	v_cvt_i32_f32_sdwa v158, v158 dst_sel:WORD_1 dst_unused:UNUSED_PAD src0_sel:DWORD
	v_cvt_i32_f32_e32 v159, v159
	v_mul_f32_e32 v152, v152, v67
	v_mul_f32_e32 v154, v154, v67
	v_mul_f32_e32 v155, v155, v67
	v_rndne_f32_e32 v153, v153
	v_or3_b32 v166, v164, v165, v166
	v_add_co_u32_e32 v164, vcc, s40, v58
	v_lshlrev_b32_e32 v161, 8, v161
	v_rndne_f32_e32 v152, v152
	v_cvt_i32_f32_e32 v153, v153
	v_rndne_f32_e32 v154, v154
	v_rndne_f32_e32 v155, v155
	v_mul_f32_e32 v149, v149, v67
	v_addc_co_u32_e32 v165, vcc, 0, v59, vcc
	v_and_b32_e32 v161, 0xff00, v161
	v_and_b32_e32 v162, 0xff0000, v162
	v_perm_b32 v160, v163, v160, s70
	s_mov_b32 s40, 0x2400000
	v_cvt_i32_f32_e32 v152, v152
	v_cvt_i32_f32_sdwa v154, v154 dst_sel:WORD_1 dst_unused:UNUSED_PAD src0_sel:DWORD
	v_cvt_i32_f32_e32 v155, v155
	v_mul_f32_e32 v148, v148, v67
	v_mul_f32_e32 v150, v150, v67
	v_mul_f32_e32 v151, v151, v67
	v_rndne_f32_e32 v149, v149
	v_or3_b32 v162, v160, v161, v162
	v_add_co_u32_e32 v160, vcc, s40, v58
	v_lshlrev_b32_e32 v157, 8, v157
	v_rndne_f32_e32 v148, v148
	v_cvt_i32_f32_e32 v149, v149
	v_rndne_f32_e32 v150, v150
	v_rndne_f32_e32 v151, v151
	v_mul_f32_e32 v145, v145, v67
	v_addc_co_u32_e32 v161, vcc, 0, v59, vcc
	v_and_b32_e32 v157, 0xff00, v157
	v_and_b32_e32 v158, 0xff0000, v158
	v_perm_b32 v156, v159, v156, s70
	s_mov_b32 s40, 0x2800000
	v_cvt_i32_f32_e32 v148, v148
	v_cvt_i32_f32_sdwa v150, v150 dst_sel:WORD_1 dst_unused:UNUSED_PAD src0_sel:DWORD
	v_cvt_i32_f32_e32 v151, v151
	v_mul_f32_e32 v144, v144, v67
	v_mul_f32_e32 v146, v146, v67
	v_mul_f32_e32 v147, v147, v67
	v_rndne_f32_e32 v145, v145
	v_or3_b32 v158, v156, v157, v158
	v_add_co_u32_e32 v156, vcc, s40, v58
	v_lshlrev_b32_e32 v153, 8, v153
	v_rndne_f32_e32 v144, v144
	v_cvt_i32_f32_e32 v145, v145
	v_rndne_f32_e32 v146, v146
	v_rndne_f32_e32 v147, v147
	v_mul_f32_e32 v141, v141, v67
	v_addc_co_u32_e32 v157, vcc, 0, v59, vcc
	v_and_b32_e32 v153, 0xff00, v153
	v_and_b32_e32 v154, 0xff0000, v154
	v_perm_b32 v152, v155, v152, s70
	v_cvt_i32_f32_e32 v144, v144
	v_cvt_i32_f32_sdwa v146, v146 dst_sel:WORD_1 dst_unused:UNUSED_PAD src0_sel:DWORD
	v_cvt_i32_f32_e32 v147, v147
	v_mul_f32_e32 v140, v140, v67
	v_mul_f32_e32 v142, v142, v67
	v_mul_f32_e32 v143, v143, v67
	v_rndne_f32_e32 v141, v141
	v_or3_b32 v154, v152, v153, v154
	v_add_co_u32_e32 v152, vcc, s71, v58
	v_lshlrev_b32_e32 v149, 8, v149
	v_rndne_f32_e32 v140, v140
	v_cvt_i32_f32_e32 v141, v141
	v_rndne_f32_e32 v142, v142
	v_rndne_f32_e32 v143, v143
	v_mul_f32_e32 v137, v137, v67
	v_addc_co_u32_e32 v153, vcc, 0, v59, vcc
	v_and_b32_e32 v149, 0xff00, v149
	v_and_b32_e32 v150, 0xff0000, v150
	v_perm_b32 v148, v151, v148, s70
	v_cvt_i32_f32_e32 v140, v140
	v_cvt_i32_f32_sdwa v142, v142 dst_sel:WORD_1 dst_unused:UNUSED_PAD src0_sel:DWORD
	v_cvt_i32_f32_e32 v143, v143
	v_mul_f32_e32 v136, v136, v67
	v_mul_f32_e32 v138, v138, v67
	v_mul_f32_e32 v139, v139, v67
	v_rndne_f32_e32 v137, v137
	v_or3_b32 v150, v148, v149, v150
	v_add_co_u32_e32 v148, vcc, s72, v58
	v_lshlrev_b32_e32 v145, 8, v145
	v_rndne_f32_e32 v136, v136
	v_cvt_i32_f32_e32 v137, v137
	v_rndne_f32_e32 v138, v138
	v_rndne_f32_e32 v139, v139
	v_addc_co_u32_e32 v149, vcc, 0, v59, vcc
	v_and_b32_e32 v145, 0xff00, v145
	v_and_b32_e32 v146, 0xff0000, v146
	v_perm_b32 v144, v147, v144, s70
	v_cvt_i32_f32_e32 v136, v136
	v_cvt_i32_f32_sdwa v138, v138 dst_sel:WORD_1 dst_unused:UNUSED_PAD src0_sel:DWORD
	v_cvt_i32_f32_e32 v139, v139
	v_or3_b32 v146, v144, v145, v146
	v_add_co_u32_e32 v144, vcc, s73, v58
	v_lshlrev_b32_e32 v141, 8, v141
	s_nop 0
	v_addc_co_u32_e32 v145, vcc, 0, v59, vcc
	v_and_b32_e32 v141, 0xff00, v141
	v_and_b32_e32 v142, 0xff0000, v142
	v_perm_b32 v140, v143, v140, s70
	v_or3_b32 v142, v140, v141, v142
	v_add_co_u32_e32 v140, vcc, s74, v58
	v_lshlrev_b32_e32 v137, 8, v137
	s_nop 0
	v_addc_co_u32_e32 v141, vcc, 0, v59, vcc
	v_and_b32_e32 v137, 0xff00, v137
	v_and_b32_e32 v138, 0xff0000, v138
	v_perm_b32 v136, v139, v136, s70
	v_or3_b32 v138, v136, v137, v138
	v_add_co_u32_e32 v136, vcc, 0x3c00000, v58
	global_store_dword v[216:217], v218, off
	s_nop 0
	v_addc_co_u32_e32 v137, vcc, 0, v59, vcc
	global_store_dword v[188:189], v190, off
	global_store_dword v[184:185], v186, off
	global_store_dword v[180:181], v182, off
	global_store_dword v[176:177], v178, off
	global_store_dword v[172:173], v174, off
	global_store_dword v[168:169], v170, off
	global_store_dword v[164:165], v166, off
	global_store_dword v[160:161], v162, off
	global_store_dword v[156:157], v158, off
	global_store_dword v[152:153], v154, off
	global_store_dword v[148:149], v150, off
	global_store_dword v[144:145], v146, off
	global_store_dword v[140:141], v142, off
	global_store_dword v[136:137], v138, off
	s_and_saveexec_b64 s[40:41], s[6:7]
	s_cbranch_execz .Lside_jB
	s_and_b64 s[38:39], s[38:39], exec
	s_cselect_b32 s38, s75, 0x8010000
	s_add_u32 s38, s33, s38
	s_addc_u32 s39, s46, 0
	s_lshl_b32 s34, s34, 2
	v_mul_f32_e32 v136, 0x3c010204, v66
	v_mov_b32_e32 v137, s34
	global_store_dword v137, v136, s[38:39]
	s_branch .Lside_jB
.Lside_jB:
	s_or_b64 exec, exec, s[40:41]
	s_cmp_lg_u32 s23, 64
	s_cbranch_scc1 .Lside_loop
